# prio1: attention passes: waves 0-3 run at s_setprio 2, waves 4-7 at 0 (each SIMD's two waves get a strict order so one's MFMA segment can overlap the other's softmax VALU); reset to 0 at the phase end
# baseline (speedup 1.0000x reference)
; __device__ __forceinline__ int v_st(int k, int c) { const int kk = (k & ~0xC) | ((k & 4) << 1) | ((k & 8) >> 1); return ((kk >> 3) * 4 + (c >> 5)) * 512 + ((kk & 7) * 32 + (c & 31)) * 2; }
; __device__ __forceinline__ int v_rd_base(int lane) { return ((lane & 3) << 3) | (((lane >> 2) & 3) << 6) | (((lane >> 4) & 1) << 5) | (((lane >> 5) & 1) << 8); }
; #define SLOAD(k0) do { vs0 = *reinterpret_cast<const bf16x8*>(&Vh[(size_t)((k0) + sr) * DM + sc]); vs1 = *reinterpret_cast<const bf16x8*>(&Vh[(size_t)((k0) + 32 + sr) * DM + sc]); \
;     ks = *reinterpret_cast<const bf16x8*>(&Kh[(size_t)((k0) + kr) * DM + kc]); } while (0)
; #define SWRITE(s) do { *(bf16x8*)(V_lds + (s) * SHM_V + vst0) = vs0; *(bf16x8*)(V_lds + (s) * SHM_V + vst1) = vs1; *(bf16x8*)(K_lds + (s) * SHM_K64 + kst) = ks; } while (0)
; #define EX2(x) x = __builtin_amdgcn_exp2f(x)
; __device__ __forceinline__ void diff_pass(const bf16_t* __restrict__ Qb, const bf16_t* __restrict__ Kh, const bf16_t* __restrict__ Vh, int seq, char* lds, f32x16 (&o)[4], const int wave_) {
;     ...
;     const bf16_t* Qw = Qb + (size_t)(wid * 32 + r32) * DM + hi * 8;
; #pragma unroll
;     for (int d0 = 0; d0 < 4; ++d0) qr[d0] = *reinterpret_cast<const bf16x8*>(Qw + d0 * 16);
;     const int sr = tid >> 4, sc = (tid & 15) * 8, vst0 = v_st(sr, sc), vst1 = v_st(32 + sr, sc);
;     const int kr = tid >> 3, kc = (tid & 7) * 8, kst = kswz<64>(kr, kc * 2);
;     const int vb0 = (int)(uintptr_t)V_lds + v_rd_base(lane);
;     bf16x8 vs0, vs1, ks;
;     ...
;     f32x16 pA0, pA1, pB0, pB1, negm; float alA, alB; bf16x8 pa0, pa1, pa2, pa3; const int NT = seq / 64;
;     int s_prev = 0, s_cur = 0, s_next = 1;
;     __syncthreads();
;     SLOAD(0); SWRITE(0); SLOAD(64); __syncthreads();
;     negm = f32x16{};
;     qkt64c(pA0, pA1, K_lds, qr, negm, r32, hi);
;     { const float pm = rowmax32(pA0, pA1); m_reg = pm; alA = 1.f;
; #pragma unroll
;       for (int r = 0; r < 16; ++r) { pA0[r] -= pm; pA1[r] -= pm; negm[r] = -pm; }
; #pragma unroll
;       for (int r = 0; r < 16; ++r) EX2(pA0[r]);
; #pragma unroll
;       for (int r = 0; r < 8; ++r) EX2(pA1[r]); }
;     SWRITE(1); __syncthreads();
.LBB0_822:
	s_lshl_b32 s0, s36, 1
	s_mov_b32 s1, -1
	s_and_b32 s64, s0, 0x700
	s_ashr_i32 s0, s37, 6
	s_lshl_b32 s2, s37, 8
	v_mbcnt_lo_u32_b32 v0, s1, 0
	v_mbcnt_hi_u32_b32 v0, s1, v0
	s_ashr_i32 s1, s0, 31
	s_lshl_b64 s[6:7], s[0:1], 11
	s_and_b32 s2, s2, 0x700
	s_or_b32 s6, s6, s2
	s_lshl_b64 s[2:3], s[6:7], 11
	v_readlane_b32 s8, v252, 16
	v_readlane_b32 s9, v252, 17
	s_add_u32 s2, s8, s2
	s_addc_u32 s3, s9, s3
	s_lshl_b32 s8, s37, 4
	s_and_b32 s38, s8, 0x380
	s_lshl_b32 s8, s38, 1
	s_add_u32 s34, s2, s8
	s_addc_u32 s35, s3, 0
	s_lshl_b64 s[10:11], s[0:1], 22
	v_readlane_b32 s0, v251, 42
	s_add_u32 s0, s0, s10
	v_readlane_b32 s1, v251, 43
	s_addc_u32 s1, s1, s11
	s_add_u32 s28, s0, s8
	s_addc_u32 s29, s1, 0
	v_readlane_b32 s0, v251, 44
	s_add_u32 s0, s0, s10
	v_readlane_b32 s1, v251, 45
	s_addc_u32 s1, s1, s11
	v_or_b32_e32 v207, s55, v0
	s_add_u32 s30, s0, s8
	s_mov_b32 s0, -1
	s_addc_u32 s31, s1, 0
	v_mbcnt_lo_u32_b32 v0, s0, 0
	v_mbcnt_hi_u32_b32 v0, s0, v0
	v_or_b32_e32 v68, s55, v0
	s_movk_i32 s0, 0xffe0
	v_ashrrev_i32_e32 v0, 1, v68
	v_bfi_b32 v0, s0, v0, v68
	v_ashrrev_i32_e32 v1, 31, v0
	v_lshlrev_b64 v[0:1], 11, v[0:1]
	v_lshrrev_b32_e32 v2, 1, v68
	v_ashrrev_i32_e32 v12, 4, v68
	v_lshl_add_u64 v[0:1], s[34:35], 0, v[0:1]
	v_and_b32_e32 v160, 16, v2
	v_lshlrev_b32_e32 v24, 3, v68
	v_ashrrev_i32_e32 v13, 31, v12
	v_lshl_add_u64 v[0:1], v[0:1], 0, v[160:161]
	v_and_b32_e32 v2, 0x78, v24
	v_lshlrev_b64 v[48:49], 11, v[12:13]
	global_load_dwordx4 v[162:165], v[0:1], off
	global_load_dwordx4 v[166:169], v[0:1], off offset:32
	global_load_dwordx4 v[170:173], v[0:1], off offset:64
	global_load_dwordx4 v[174:177], v[0:1], off offset:96
	v_lshl_add_u64 v[0:1], s[30:31], 0, v[48:49]
	v_lshlrev_b32_e32 v4, 1, v2
	v_mov_b32_e32 v5, v161
	v_add_u32_e32 v14, 32, v12
	v_ashrrev_i32_e32 v16, 3, v68
	v_lshl_add_u64 v[18:19], v[0:1], 0, v[4:5]
	s_barrier
	global_load_dwordx4 v[0:3], v[18:19], off
	v_ashrrev_i32_e32 v15, 31, v14
	v_ashrrev_i32_e32 v17, 31, v16
	v_lshlrev_b32_e32 v64, 4, v68
	v_lshlrev_b64 v[6:7], 11, v[14:15]
	v_lshlrev_b64 v[50:51], 11, v[16:17]
	v_lshl_add_u64 v[6:7], s[30:31], 0, v[6:7]
	v_and_b32_e32 v20, 0x70, v64
	v_lshl_add_u64 v[8:9], s[28:29], 0, v[50:51]
	v_mov_b32_e32 v21, v161
	v_lshl_add_u64 v[4:5], v[6:7], 0, v[4:5]
	v_lshl_add_u64 v[22:23], v[8:9], 0, v[20:21]
	global_load_dwordx4 v[4:7], v[4:5], off
	v_and_b32_e32 v13, 0xfffff0, v12
	global_load_dwordx4 v[8:11], v[22:23], off
	v_add_co_u32_e32 v194, vcc, 0x20000, v18
	s_nop 1
	v_addc_co_u32_e32 v195, vcc, 0, v19, vcc
	global_load_dwordx4 v[52:55], v[194:195], off
	v_add_co_u32_e32 v194, vcc, 0x30000, v18
	s_nop 1
	v_addc_co_u32_e32 v195, vcc, 0, v19, vcc
	global_load_dwordx4 v[56:59], v[194:195], off
	v_add_co_u32_e32 v194, vcc, 0x20000, v22
	s_nop 1
	v_addc_co_u32_e32 v195, vcc, 0, v23, vcc
	global_load_dwordx4 v[60:63], v[194:195], off
	v_lshlrev_b32_e32 v15, 1, v12
	v_and_or_b32 v13, v15, 8, v13
	v_lshrrev_b32_e32 v15, 1, v12
	v_lshrrev_b32_e32 v13, 1, v13
	v_bfe_u32 v17, v24, 5, 2
	v_and_b32_e32 v12, 3, v12
	v_or_b32_e32 v13, v13, v17
	v_and_or_b32 v12, v15, 4, v12
	v_lshlrev_b32_e32 v13, 9, v13
	v_lshlrev_b32_e32 v12, 6, v12
	v_and_b32_e32 v15, 48, v64
	v_or3_b32 v218, v13, v12, v15
	v_and_b32_e32 v13, 0xfffff0, v14
	v_lshlrev_b32_e32 v14, 1, v14
	v_and_or_b32 v13, v14, 8, v13
	v_lshrrev_b32_e32 v13, 1, v13
	v_or_b32_e32 v13, v13, v17
	v_add_u32_e32 v70, 0, v218
	s_mov_b32 s0, 0x20000
	v_lshlrev_b32_e32 v13, 9, v13
	v_or3_b32 v219, v13, v12, v15
	v_lshlrev_b32_e32 v12, 7, v16
	v_and_b32_e32 v13, 0x70, v68
	s_mov_b32 s1, 0x30000
	v_bitop3_b32 v220, v20, v12, v13 bitop3:0xde
	v_add_u32_e32 v71, 0, v219
	v_add_u32_e32 v221, 0, v220
	v_and_b32_e32 v69, 31, v68
	v_lshlrev_b32_e32 v12, 7, v69
	v_and_b32_e32 v13, 0x70, v24
	v_bitop3_b32 v223, v160, v12, v13 bitop3:0xde
	v_add_u32_e32 v222, 0, v223
	s_add_i32 s39, 0, 0x12000
	v_and_b32_e32 v72, 63, v68
	s_mov_b32 s12, 0
	s_mov_b32 s13, s12
	s_mov_b32 s14, s12
	s_mov_b32 s15, s12
	s_mov_b32 s16, s12
	s_mov_b32 s17, s12
	s_mov_b32 s18, s12
	s_mov_b32 s19, s12
	s_mov_b32 s20, s12
	s_mov_b32 s21, s12
	s_mov_b32 s22, s12
	s_mov_b32 s23, s12
	s_mov_b32 s24, s12
	s_mov_b32 s25, s12
	s_mov_b32 s26, s12
	s_mov_b32 s27, s12
	s_cmp_lg_u32 0, -1
	s_mov_b32 s42, 1
	s_mov_b32 s40, -1
	s_mov_b32 s41, 2
	v_mov_b32_e32 v230, 1.0
	v_mov_b32_e32 v215, 0
	s_waitcnt vmcnt(5)
	ds_write_b128 v70, v[0:3]
	s_waitcnt vmcnt(4)
	ds_write_b128 v71, v[4:7]
	s_waitcnt vmcnt(3)
	ds_write_b128 v221, v[8:11] offset:49152
	v_and_b32_e32 v8, 0x3fffffc0, v68
	s_waitcnt lgkmcnt(0)
	s_barrier
	ds_read_b128 v[0:3], v222 offset:49152
	ds_read_b128 v[4:7], v222 offset:53248
	s_waitcnt lgkmcnt(1)
	v_mfma_f32_32x32x16_bf16 v[16:31], v[0:3], v[162:165], 0
	v_or_b32_e32 v0, 32, v160
	v_bitop3_b32 v226, v0, v12, v13 bitop3:0xde
	v_add_u32_e32 v224, 0, v226
	ds_read_b128 v[0:3], v224 offset:49152
	v_lshl_add_u32 v213, v8, 2, s39
	s_cselect_b32 s0, 0, 0
	v_lshl_add_u32 v214, v69, 2, v213
	s_waitcnt lgkmcnt(1)
	v_mfma_f32_32x32x16_bf16 v[32:47], v[4:7], v[162:165], 0
	ds_read_b128 v[4:7], v224 offset:53248
	s_waitcnt lgkmcnt(1)
	v_mfma_f32_32x32x16_bf16 v[16:31], v[0:3], v[166:169], v[16:31]
	v_or_b32_e32 v0, 64, v160
	v_bitop3_b32 v228, v0, v12, v13 bitop3:0xde
	v_add_u32_e32 v225, 0, v228
	ds_read_b128 v[0:3], v225 offset:53248
	ds_read_b128 v[8:11], v225 offset:49152
	s_waitcnt lgkmcnt(2)
	v_mfma_f32_32x32x16_bf16 v[32:47], v[4:7], v[166:169], v[32:47]
	v_lshlrev_b32_e32 v4, 3, v72
	v_and_b32_e32 v5, 0xc0, v64
	v_lshlrev_b32_e32 v6, 1, v68
	v_and_or_b32 v5, v4, 24, v5
	v_and_b32_e32 v6, 32, v6
	v_and_b32_e32 v4, 0x100, v4
	v_or3_b32 v216, v5, v6, v4
	s_waitcnt lgkmcnt(0)
	v_mfma_f32_32x32x16_bf16 v[16:31], v[8:11], v[170:173], v[16:31]
	v_or_b32_e32 v4, 0x60, v160
	v_bitop3_b32 v229, v4, v12, v13 bitop3:0xde
	v_add_u32_e32 v227, 0, v229
	ds_read_b128 v[64:67], v227 offset:53248
	ds_read_b128 v[4:7], v227 offset:49152
	s_waitcnt vmcnt(2)
	ds_write_b128 v70, v[52:55] offset:16384
	s_waitcnt vmcnt(1)
	ds_write_b128 v71, v[56:59] offset:16384
	s_waitcnt vmcnt(0)
	ds_write_b128 v221, v[60:63] offset:57344
	v_mfma_f32_32x32x16_bf16 v[32:47], v[0:3], v[170:173], v[32:47]
	v_add_u32_e32 v217, s0, v216
	v_cmp_gt_u32_e64 s[0:1], 32, v72
	s_waitcnt lgkmcnt(0)
	s_barrier
; #define EX2(x) x = __builtin_amdgcn_exp2f(x)
; __device__ __forceinline__ void diff_pass(const bf16_t* __restrict__ Qb, const bf16_t* __restrict__ Kh, const bf16_t* __restrict__ Vh, int seq, char* lds, f32x16 (&o)[4], const int wave_) {
;     ...
;     negm = f32x16{};
;     qkt64c(pA0, pA1, K_lds, qr, negm, r32, hi);
;     { const float pm = rowmax32(pA0, pA1); m_reg = pm; alA = 1.f;
; #pragma unroll
;       for (int r = 0; r < 16; ++r) { pA0[r] -= pm; pA1[r] -= pm; negm[r] = -pm; }
; #pragma unroll
;       for (int r = 0; r < 16; ++r) EX2(pA0[r]);
; #pragma unroll
;       for (int r = 0; r < 8; ++r) EX2(pA1[r]); }
	v_mfma_f32_32x32x16_bf16 v[16:31], v[4:7], v[174:177], v[16:31]
	v_mov_b64_e32 v[0:1], s[12:13]
	v_mov_b64_e32 v[14:15], s[26:27]
	v_mov_b64_e32 v[2:3], s[14:15]
	v_mov_b64_e32 v[4:5], s[16:17]
	v_mov_b64_e32 v[6:7], s[18:19]
	v_mov_b64_e32 v[8:9], s[20:21]
	v_mov_b64_e32 v[10:11], s[22:23]
	v_mfma_f32_32x32x16_bf16 v[32:47], v[64:67], v[174:177], v[32:47]
	s_nop 3
	v_max_f32_e32 v64, v17, v17
	v_max_f32_e32 v65, v16, v16
	v_max_f32_e32 v64, v65, v64
	v_mov_b64_e32 v[12:13], s[24:25]
	s_nop 3
	v_max3_f32 v65, v18, v19, v33
	v_max3_f32 v64, v64, v32, v34
	v_max3_f32 v64, v64, v35, v20
	v_max3_f32 v65, v65, v22, v23
	v_max3_f32 v64, v64, v21, v36
	v_max3_f32 v65, v65, v38, v39
	v_max3_f32 v64, v64, v37, v24
	v_max3_f32 v65, v65, v26, v27
	v_max3_f32 v64, v64, v25, v40
	v_max3_f32 v65, v65, v42, v43
	v_max3_f32 v64, v64, v41, v28
	v_max3_f32 v65, v65, v30, v31
	v_max3_f32 v64, v64, v29, v44
	v_max3_f32 v65, v65, v46, v47
	v_max3_f32 v64, v64, v45, v65
	v_mov_b32_e32 v65, v64
	s_nop 1
	v_permlane32_swap_b32_e32 v64, v65
	v_max_f32_e32 v65, v65, v65
	v_max_f32_e32 v64, v64, v64
	v_max_f32_e32 v196, v64, v65
	v_sub_f32_e32 v16, v16, v196
	v_sub_f32_e32 v17, v17, v196
	v_sub_f32_e32 v18, v18, v196
	v_exp_f32_e32 v96, v16
	v_exp_f32_e32 v97, v17
	v_exp_f32_e32 v98, v18
	v_lshl_add_u64 v[16:17], s[10:11], 0, v[50:51]
	v_and_b32_e32 v18, 7, v68
	v_sub_f32_e32 v32, v32, v196
	v_sub_f32_e32 v33, v33, v196
	v_sub_f32_e32 v34, v34, v196
	v_sub_f32_e32 v19, v19, v196
	v_sub_f32_e32 v35, v35, v196
	v_sub_f32_e32 v20, v20, v196
	v_sub_f32_e32 v36, v36, v196
	v_sub_f32_e32 v21, v21, v196
	v_sub_f32_e32 v37, v37, v196
	v_sub_f32_e32 v22, v22, v196
	v_sub_f32_e32 v38, v38, v196
	v_sub_f32_e32 v23, v23, v196
	v_sub_f32_e32 v39, v39, v196
	v_sub_f32_e32 v24, v24, v196
	v_sub_f32_e32 v25, v25, v196
	v_sub_f32_e32 v26, v26, v196
	v_sub_f32_e32 v27, v27, v196
	v_sub_f32_e32 v28, v28, v196
	v_sub_f32_e32 v29, v29, v196
	v_sub_f32_e32 v30, v30, v196
	v_sub_f32_e32 v31, v31, v196
	v_lshl_or_b32 v16, v18, 4, v16
	v_exp_f32_e32 v99, v19
	v_exp_f32_e32 v100, v20
	v_exp_f32_e32 v101, v21
	v_exp_f32_e32 v102, v22
	v_exp_f32_e32 v103, v23
	v_exp_f32_e32 v104, v24
	v_exp_f32_e32 v105, v25
	v_exp_f32_e32 v106, v26
	v_exp_f32_e32 v107, v27
	v_exp_f32_e32 v108, v28
	v_exp_f32_e32 v109, v29
	v_exp_f32_e32 v110, v30
	v_exp_f32_e32 v111, v31
	v_exp_f32_e32 v112, v32
	v_exp_f32_e32 v113, v33
	v_exp_f32_e32 v114, v34
	v_exp_f32_e32 v115, v35
	v_exp_f32_e32 v116, v36
	v_exp_f32_e32 v117, v37
	v_exp_f32_e32 v118, v38
	v_exp_f32_e32 v119, v39
	v_lshl_add_u64 v[198:199], s[52:53], 0, v[16:17]
	v_lshl_add_u64 v[16:17], s[10:11], 0, v[48:49]
	v_and_b32_e32 v18, 15, v68
	v_lshl_or_b32 v16, v18, 4, v16
	v_xor_b32_e32 v80, 0x80000000, v196
	v_pk_add_f32 v[120:121], v[40:41], v[196:197] op_sel_hi:[1,0] neg_lo:[0,1] neg_hi:[0,1]
	v_pk_add_f32 v[122:123], v[42:43], v[196:197] op_sel_hi:[1,0] neg_lo:[0,1] neg_hi:[0,1]
	v_pk_add_f32 v[124:125], v[44:45], v[196:197] op_sel_hi:[1,0] neg_lo:[0,1] neg_hi:[0,1]
	v_pk_add_f32 v[126:127], v[46:47], v[196:197] op_sel_hi:[1,0] neg_lo:[0,1] neg_hi:[0,1]
	v_lshl_add_u64 v[200:201], s[52:53], 0, v[16:17]
	s_add_u32 s14, s52, s10
	s_addc_u32 s15, s53, s11
	s_add_u32 s14, s14, s64
	s_addc_u32 s15, s15, s65
	s_add_u32 s16, s14, 0x8a40000
	s_addc_u32 s17, s15, 0
	s_add_u32 s14, s14, 0x6a40000
	s_addc_u32 s15, s15, 0
	s_lshl_b32 s18, s55, 4
	s_cmp_lt_u32 s18, 0x1000
	s_cbranch_scc0 .Lprio_p1_skip
	s_setprio 2
.Lprio_p1_skip:
	v_lshrrev_b32_e32 v194, 4, v207
	v_xor_b32_e32 v194, v194, v207
	v_and_b32_e32 v194, 7, v194
	v_lshrrev_b32_e32 v195, 3, v207
	v_lshlrev_b32_e32 v195, 11, v195
	v_lshl_or_b32 v194, v194, 4, v195
	v_lshrrev_b32_e32 v195, 2, v207
	v_and_b32_e32 v195, 7, v195
	v_and_b32_e32 v255, 3, v195
	v_lshrrev_b32_e32 v195, 2, v195
	v_lshl_or_b32 v255, v195, 3, v255
	v_lshrrev_b32_e32 v195, 7, v207
	v_and_b32_e32 v195, 1, v195
	v_lshl_or_b32 v255, v195, 2, v255
	v_lshrrev_b32_e32 v195, 8, v207
	v_lshl_or_b32 v255, v195, 4, v255
	v_lshlrev_b32_e32 v255, 11, v255
	v_lshrrev_b32_e32 v195, 5, v207
	v_and_b32_e32 v195, 3, v195
	v_lshl_or_b32 v255, v195, 6, v255
	v_and_b32_e32 v195, 3, v207
	v_lshl_or_b32 v195, v195, 4, v255
	v_add_u32_e32 v255, 0x10000, v195
	v_mov_b64_e32 v[62:63], v[14:15]
	v_mov_b64_e32 v[46:47], v[14:15]
	v_mov_b64_e32 v[30:31], v[14:15]
	v_mov_b64_e32 v[60:61], v[12:13]
	v_mov_b64_e32 v[58:59], v[10:11]
	v_mov_b64_e32 v[56:57], v[8:9]
	v_mov_b64_e32 v[54:55], v[6:7]
	v_mov_b64_e32 v[52:53], v[4:5]
	v_mov_b64_e32 v[50:51], v[2:3]
	v_mov_b64_e32 v[48:49], v[0:1]
	v_mov_b64_e32 v[44:45], v[12:13]
	v_mov_b64_e32 v[42:43], v[10:11]
	v_mov_b64_e32 v[40:41], v[8:9]
	v_mov_b64_e32 v[38:39], v[6:7]
	v_mov_b64_e32 v[36:37], v[4:5]
	v_mov_b64_e32 v[34:35], v[2:3]
	v_mov_b64_e32 v[32:33], v[0:1]
	v_mov_b64_e32 v[28:29], v[12:13]
	v_mov_b64_e32 v[26:27], v[10:11]
	v_mov_b64_e32 v[24:25], v[8:9]
	v_mov_b64_e32 v[22:23], v[6:7]
	v_mov_b64_e32 v[20:21], v[4:5]
	v_mov_b64_e32 v[18:19], v[2:3]
	v_mov_b64_e32 v[16:17], v[0:1]
	v_mov_b32_e32 v81, v80
	v_mov_b32_e32 v82, v80
	v_mov_b32_e32 v83, v80
	v_mov_b32_e32 v84, v80
	v_mov_b32_e32 v85, v80
	v_mov_b32_e32 v86, v80
	v_mov_b32_e32 v87, v80
	v_mov_b32_e32 v88, v80
	v_mov_b32_e32 v89, v80
	v_mov_b32_e32 v90, v80
	v_mov_b32_e32 v91, v80
	v_mov_b32_e32 v92, v80
	v_mov_b32_e32 v93, v80
	v_mov_b32_e32 v94, v80
	v_mov_b32_e32 v95, v80

; __device__ __forceinline__ unsigned cvt_pk_bf16(float lo, float hi) { unsigned r; asm volatile("v_cvt_pk_bf16_f32 %0, %1, %2" : "=v"(r) : "v"(lo), "v"(hi)); return r; }
; #define SBAR() __builtin_amdgcn_sched_barrier(0)
; __device__ __forceinline__ int crow(int r, int hi) { return (r & 3) + 8 * (r >> 2) + 4 * hi; }
; #define RESC(a) do { if (__any((a) < 1.f)) { if (hi == 0) al_l[r32] = (a); asm volatile("s_waitcnt lgkmcnt(0)" ::: "memory"); \
;     _Pragma("unroll") for (int d = 0; d < 4; ++d) _Pragma("unroll") for (int r = 0; r < 16; ++r) o[d][r] *= al_l[crow(r, hi)]; } } while (0)
; __device__ __forceinline__ void diff_pass(const bf16_t* __restrict__ Qb, const bf16_t* __restrict__ Kh, const bf16_t* __restrict__ Vh, int seq, char* lds, f32x16 (&o)[4], const int wave_) {
;     ...
;     SBAR(); qkt64c(pB0, pB1, K_lds + s_cur * SHM_K64, qr, negm, r32, hi); FIN(pA0, pA1, alA); SBAR();
;     YSEG(pB0, pB1, alB, s_prev);
;     RESC(alB);
;     FIN(pB0, pB1, alB); SBAR();
;     pv_d0(o, vb0 + s_cur * SHM_V, pa0, pa1, pa2, pa3);
;     if (hi == 0) li_l[r32] = l_reg; asm volatile("s_waitcnt lgkmcnt(0)" ::: "memory");
; #pragma unroll
;     for (int r = 0; r < 16; ++r) { const float rl = __builtin_amdgcn_rcpf(li_l[crow(r, hi)]);
; #pragma unroll
;         for (int d = 0; d < 4; ++d) o[d][r] *= rl; }
; __device__ __forceinline__ void diff_unit(int b, int h, int qb, const bf16_t* Q, const bf16_t* K, const bf16_t* V, bf16_t* YA, float lam, float omli, const float* subln, char* lds, const int wave_) {
;     ...
;     unsigned* park = (unsigned*)(lds + DA_LDS) + wid * 2048 + lane;
; #pragma unroll
;     for (int d = 0; d < 4; ++d)
; #pragma unroll
;         for (int r = 0; r < 8; ++r) park[(d * 8 + r) * 64] = cvt_pk_bf16(o[d][2 * r], o[d][2 * r + 1]);
.LBB0_843:
	v_exp_f32_e32 v96, v72
	v_exp_f32_e32 v97, v73
	v_add_f32_e32 v72, v80, v81
	v_add_f32_e32 v73, v82, v83
	v_exp_f32_e32 v98, v74
	v_add_f32_e32 v72, v72, v73
	v_add_f32_e32 v73, v84, v85
	v_add_f32_e32 v74, v86, v87
	v_exp_f32_e32 v99, v75
	v_add_f32_e32 v73, v73, v74
	v_add_f32_e32 v74, v88, v89
	v_add_f32_e32 v75, v90, v91
	v_exp_f32_e32 v100, v76
	v_add_f32_e32 v74, v74, v75
	v_add_f32_e32 v75, v92, v93
	v_add_f32_e32 v76, v94, v95
	v_exp_f32_e32 v101, v77
	v_add_f32_e32 v75, v75, v76
	v_add_f32_e32 v76, v64, v65
	v_add_f32_e32 v77, v66, v67
	v_add_f32_e32 v76, v76, v77
	v_exp_f32_e32 v102, v78
	v_exp_f32_e32 v103, v79
	v_add_f32_e32 v72, v72, v76
	v_add_f32_e32 v76, v68, v69
	v_add_f32_e32 v77, v70, v71
	v_add_f32_e32 v76, v76, v77
	v_add_f32_e32 v73, v73, v76
	v_add_f32_e32 v76, v96, v97
	v_add_f32_e32 v77, v98, v99
	v_add_f32_e32 v76, v76, v77
	v_add_f32_e32 v74, v74, v76
	v_add_f32_e32 v76, v100, v101
	v_add_f32_e32 v77, v102, v103
	v_add_f32_e32 v76, v76, v77
	v_add_f32_e32 v75, v75, v76
	v_add_f32_e32 v72, v72, v73
	v_add_f32_e32 v73, v74, v75
	v_add_f32_e32 v72, v72, v73
	v_mov_b32_e32 v73, v72
	s_nop 1
	v_permlane32_swap_b32_e32 v72, v73
	v_cvt_pk_bf16_f32 v74, v80, v81
	v_cvt_pk_bf16_f32 v75, v82, v83
	v_cvt_pk_bf16_f32 v76, v84, v85
	v_cvt_pk_bf16_f32 v77, v86, v87
	v_cvt_pk_bf16_f32 v78, v88, v89
	v_cvt_pk_bf16_f32 v79, v90, v91
	v_cvt_pk_bf16_f32 v80, v92, v93
	v_cvt_pk_bf16_f32 v81, v94, v95
	v_cvt_pk_bf16_f32 v64, v64, v65
	v_cvt_pk_bf16_f32 v65, v66, v67
	v_cvt_pk_bf16_f32 v66, v68, v69
	v_cvt_pk_bf16_f32 v67, v70, v71
	v_cvt_pk_bf16_f32 v68, v96, v97
	v_cvt_pk_bf16_f32 v69, v98, v99
	v_cvt_pk_bf16_f32 v70, v100, v101
	v_cvt_pk_bf16_f32 v71, v102, v103
	s_nop 0
	v_permlane32_swap_b32_e32 v74, v76
	v_permlane32_swap_b32_e32 v75, v77
	v_permlane32_swap_b32_e32 v78, v80
	v_permlane32_swap_b32_e32 v79, v81
	v_permlane32_swap_b32_e32 v64, v66
	v_permlane32_swap_b32_e32 v65, v67
	v_permlane32_swap_b32_e32 v68, v70
	v_permlane32_swap_b32_e32 v69, v71
	s_cmp_lg_u32 0, -1
	s_cselect_b32 s2, 0, 0
	s_addk_i32 s2, 0x4000
	v_add_u32_e32 v98, s2, v216
	ds_read_b64_tr_b16 v[82:83], v98 offset:0
	ds_read_b64_tr_b16 v[84:85], v98 offset:0x800
	ds_read_b64_tr_b16 v[86:87], v98 offset:0x1000
	ds_read_b64_tr_b16 v[88:89], v98 offset:0x1800
	ds_read_b64_tr_b16 v[90:91], v98 offset:0x2000
	ds_read_b64_tr_b16 v[92:93], v98 offset:0x2800
	ds_read_b64_tr_b16 v[94:95], v98 offset:0x3000
	ds_read_b64_tr_b16 v[96:97], v98 offset:0x3800
	s_waitcnt lgkmcnt(0)
	s_nop 0
	v_mfma_f32_32x32x16_bf16 v[0:15], v[74:77], v[82:85], v[0:15]
	ds_read_b64_tr_b16 v[82:83], v98 offset:0x200
	ds_read_b64_tr_b16 v[84:85], v98 offset:0xa00
	v_mfma_f32_32x32x16_bf16 v[0:15], v[78:81], v[86:89], v[0:15]
	ds_read_b64_tr_b16 v[86:87], v98 offset:0x1200
	ds_read_b64_tr_b16 v[88:89], v98 offset:0x1a00
	v_mfma_f32_32x32x16_bf16 v[0:15], v[64:67], v[90:93], v[0:15]
	ds_read_b64_tr_b16 v[90:91], v98 offset:0x2200
	ds_read_b64_tr_b16 v[92:93], v98 offset:0x2a00
	v_mfma_f32_32x32x16_bf16 v[0:15], v[68:71], v[94:97], v[0:15]
	ds_read_b64_tr_b16 v[94:95], v98 offset:0x3200
	ds_read_b64_tr_b16 v[96:97], v98 offset:0x3a00
	s_waitcnt lgkmcnt(0)
	v_mfma_f32_32x32x16_bf16 v[48:63], v[74:77], v[82:85], v[48:63]
	ds_read_b64_tr_b16 v[82:83], v98 offset:0x400
	ds_read_b64_tr_b16 v[84:85], v98 offset:0xc00
	v_mfma_f32_32x32x16_bf16 v[48:63], v[78:81], v[86:89], v[48:63]
	ds_read_b64_tr_b16 v[86:87], v98 offset:0x1400
	ds_read_b64_tr_b16 v[88:89], v98 offset:0x1c00
	v_mfma_f32_32x32x16_bf16 v[48:63], v[64:67], v[90:93], v[48:63]
	ds_read_b64_tr_b16 v[90:91], v98 offset:0x2400
	ds_read_b64_tr_b16 v[92:93], v98 offset:0x2c00
	v_mfma_f32_32x32x16_bf16 v[48:63], v[68:71], v[94:97], v[48:63]
	ds_read_b64_tr_b16 v[94:95], v98 offset:0x3400
	ds_read_b64_tr_b16 v[96:97], v98 offset:0x3c00
	s_waitcnt lgkmcnt(0)
	v_mfma_f32_32x32x16_bf16 v[32:47], v[74:77], v[82:85], v[32:47]
	ds_read_b64_tr_b16 v[82:83], v98 offset:0x600
	ds_read_b64_tr_b16 v[84:85], v98 offset:0xe00
	v_mfma_f32_32x32x16_bf16 v[32:47], v[78:81], v[86:89], v[32:47]
	ds_read_b64_tr_b16 v[86:87], v98 offset:0x1600
	ds_read_b64_tr_b16 v[88:89], v98 offset:0x1e00
	v_mfma_f32_32x32x16_bf16 v[32:47], v[64:67], v[90:93], v[32:47]
	ds_read_b64_tr_b16 v[90:91], v98 offset:0x2600
	ds_read_b64_tr_b16 v[92:93], v98 offset:0x2e00
	v_mfma_f32_32x32x16_bf16 v[32:47], v[68:71], v[94:97], v[32:47]
	ds_read_b64_tr_b16 v[94:95], v98 offset:0x3600
	ds_read_b64_tr_b16 v[96:97], v98 offset:0x3e00
	s_waitcnt lgkmcnt(0)
	v_mfma_f32_32x32x16_bf16 v[16:31], v[74:77], v[82:85], v[16:31]
	v_mfma_f32_32x32x16_bf16 v[16:31], v[78:81], v[86:89], v[16:31]
	v_mfma_f32_32x32x16_bf16 v[16:31], v[64:67], v[90:93], v[16:31]
	v_mfma_f32_32x32x16_bf16 v[16:31], v[68:71], v[94:97], v[16:31]
	s_and_saveexec_b64 s[12:13], s[0:1]
	v_add_f32_e32 v64, v128, v129
	v_fmac_f32_e32 v64, v215, v202
	v_add_f32_e32 v65, v72, v73
	v_fmac_f32_e32 v65, v64, v130
	ds_write_b32 v214, v65
	s_or_b64 exec, exec, s[12:13]
	s_waitcnt lgkmcnt(0)
	v_add_u32_e32 v72, v213, v160
	ds_read_b128 v[64:67], v72
	ds_read_b128 v[68:71], v72 offset:32
	v_ashrrev_i32_e32 v214, 6, v207
	s_add_i32 s0, 0, 0x12800
	v_and_b32_e32 v213, 63, v207
	s_waitcnt lgkmcnt(1)
	v_rcp_f32_e32 v64, v64
	v_rcp_f32_e32 v65, v65
	v_lshl_add_u32 v215, v214, 13, s0
	v_lshl_add_u32 v216, v213, 2, v215
	v_mul_f32_e32 v73, v0, v64
	v_rcp_f32_e32 v0, v66
	v_mul_f32_e32 v48, v48, v64
	v_mul_f32_e32 v32, v32, v64
	v_mul_f32_e32 v16, v16, v64
	v_mul_f32_e32 v64, v1, v65
	v_mul_f32_e32 v49, v49, v65
	v_mul_f32_e32 v33, v33, v65
	v_mul_f32_e32 v17, v17, v65
	v_mul_f32_e32 v65, v2, v0
	v_rcp_f32_e32 v1, v67
	v_mul_f32_e32 v50, v50, v0
	v_mul_f32_e32 v34, v34, v0
	v_mul_f32_e32 v18, v18, v0
	s_waitcnt lgkmcnt(0)
; __device__ __forceinline__ unsigned cvt_pk_bf16(float lo, float hi) { unsigned r; asm volatile("v_cvt_pk_bf16_f32 %0, %1, %2" : "=v"(r) : "v"(lo), "v"(hi)); return r; }
; __device__ __forceinline__ int crow(int r, int hi) { return (r & 3) + 8 * (r >> 2) + 4 * hi; }
; __device__ __forceinline__ void diff_pass(const bf16_t* __restrict__ Qb, const bf16_t* __restrict__ Kh, const bf16_t* __restrict__ Vh, int seq, char* lds, f32x16 (&o)[4], const int wave_) {
;     ...
;     if (hi == 0) li_l[r32] = l_reg; asm volatile("s_waitcnt lgkmcnt(0)" ::: "memory");
; #pragma unroll
;     for (int r = 0; r < 16; ++r) { const float rl = __builtin_amdgcn_rcpf(li_l[crow(r, hi)]);
; #pragma unroll
;         for (int d = 0; d < 4; ++d) o[d][r] *= rl; }
; __device__ __forceinline__ void diff_unit(int b, int h, int qb, const bf16_t* Q, const bf16_t* K, const bf16_t* V, bf16_t* YA, float lam, float omli, const float* subln, char* lds, const int wave_) {
;     ...
;     unsigned* park = (unsigned*)(lds + DA_LDS) + wid * 2048 + lane;
; #pragma unroll
;     for (int d = 0; d < 4; ++d)
; #pragma unroll
;         for (int r = 0; r < 8; ++r) park[(d * 8 + r) * 64] = cvt_pk_bf16(o[d][2 * r], o[d][2 * r + 1]);
;     diff_pass(Qb + 64, Kh + 64, Vh, SEQ, lds, o, wave_);
	v_rcp_f32_e32 v0, v68
	v_mul_f32_e32 v66, v3, v1
	v_mul_f32_e32 v51, v51, v1
	v_mul_f32_e32 v35, v35, v1
	v_mul_f32_e32 v19, v19, v1
	v_mul_f32_e32 v67, v4, v0
	v_rcp_f32_e32 v1, v69
	v_rcp_f32_e32 v4, v70
	v_rcp_f32_e32 v70, v71
	v_mul_f32_e32 v52, v52, v0
	v_mul_f32_e32 v36, v36, v0
	v_mul_f32_e32 v20, v20, v0
	v_mul_f32_e32 v68, v5, v1
	v_mul_f32_e32 v53, v53, v1
	v_mul_f32_e32 v37, v37, v1
	v_mul_f32_e32 v21, v21, v1
	v_mul_f32_e32 v69, v6, v4
	v_mul_f32_e32 v54, v54, v4
	ds_read_b128 v[0:3], v72 offset:64
	v_mul_f32_e32 v38, v38, v4
	v_mul_f32_e32 v22, v22, v4
	v_mul_f32_e32 v71, v7, v70
	ds_read_b128 v[4:7], v72 offset:96
	s_waitcnt lgkmcnt(1)
	v_rcp_f32_e32 v0, v0
	v_rcp_f32_e32 v1, v1
	v_rcp_f32_e32 v2, v2
	v_rcp_f32_e32 v3, v3
	s_waitcnt lgkmcnt(0)
	v_rcp_f32_e32 v4, v4
	v_rcp_f32_e32 v5, v5
	v_rcp_f32_e32 v6, v6
	v_rcp_f32_e32 v7, v7
	v_mul_f32_e32 v8, v8, v0
	v_mul_f32_e32 v56, v56, v0
	v_mul_f32_e32 v40, v40, v0
	v_mul_f32_e32 v0, v24, v0
	v_mul_f32_e32 v9, v9, v1
	v_mul_f32_e32 v24, v57, v1
	v_mul_f32_e32 v41, v41, v1
	v_mul_f32_e32 v1, v25, v1
	v_mul_f32_e32 v10, v10, v2
	v_mul_f32_e32 v25, v58, v2
	v_mul_f32_e32 v42, v42, v2
	v_mul_f32_e32 v2, v26, v2
	v_mul_f32_e32 v11, v11, v3
	v_mul_f32_e32 v26, v59, v3
	v_mul_f32_e32 v43, v43, v3
	v_mul_f32_e32 v3, v27, v3
	v_mul_f32_e32 v12, v12, v4
	v_mul_f32_e32 v27, v60, v4
	v_mul_f32_e32 v44, v44, v4
	v_mul_f32_e32 v4, v28, v4
	v_mul_f32_e32 v13, v13, v5
	v_mul_f32_e32 v28, v61, v5
	v_mul_f32_e32 v45, v45, v5
	v_mul_f32_e32 v5, v29, v5
	v_mul_f32_e32 v14, v14, v6
	v_mul_f32_e32 v29, v62, v6
	v_mul_f32_e32 v46, v46, v6
	v_mul_f32_e32 v6, v30, v6
	v_mul_f32_e32 v15, v15, v7
	v_mul_f32_e32 v30, v63, v7
	v_mul_f32_e32 v47, v47, v7
	v_mul_f32_e32 v7, v31, v7
	v_cvt_pk_bf16_f32 v31, v73, v64
	ds_write_b32 v216, v31
	v_cvt_pk_bf16_f32 v31, v65, v66
	ds_write_b32 v216, v31 offset:256
	v_cvt_pk_bf16_f32 v31, v67, v68
	ds_write_b32 v216, v31 offset:512
	v_cvt_pk_bf16_f32 v31, v69, v71
	ds_write_b32 v216, v31 offset:768
	v_cvt_pk_bf16_f32 v8, v8, v9
	ds_write_b32 v216, v8 offset:1024
	v_cvt_pk_bf16_f32 v8, v10, v11
	ds_write_b32 v216, v8 offset:1280
	v_cvt_pk_bf16_f32 v8, v12, v13
	ds_write_b32 v216, v8 offset:1536
	v_cvt_pk_bf16_f32 v8, v14, v15
	ds_write_b32 v216, v8 offset:1792
	v_cvt_pk_bf16_f32 v8, v48, v49
	ds_write_b32 v216, v8 offset:2048
	v_cvt_pk_bf16_f32 v8, v50, v51
	ds_write_b32 v216, v8 offset:2304
	v_cvt_pk_bf16_f32 v8, v52, v53
	v_mul_f32_e32 v55, v55, v70
	ds_write_b32 v216, v8 offset:2560
	v_cvt_pk_bf16_f32 v8, v54, v55
	ds_write_b32 v216, v8 offset:2816
	v_cvt_pk_bf16_f32 v8, v56, v24
	ds_write_b32 v216, v8 offset:3072
	v_cvt_pk_bf16_f32 v8, v25, v26
	ds_write_b32 v216, v8 offset:3328
	v_cvt_pk_bf16_f32 v8, v27, v28
	ds_write_b32 v216, v8 offset:3584
	v_cvt_pk_bf16_f32 v8, v29, v30
	ds_write_b32 v216, v8 offset:3840
	v_cvt_pk_bf16_f32 v8, v32, v33
	ds_write_b32 v216, v8 offset:4096
	v_cvt_pk_bf16_f32 v8, v34, v35
	ds_write_b32 v216, v8 offset:4352
	v_cvt_pk_bf16_f32 v8, v36, v37
	v_mul_f32_e32 v39, v39, v70
	ds_write_b32 v216, v8 offset:4608
	v_cvt_pk_bf16_f32 v8, v38, v39
	ds_write_b32 v216, v8 offset:4864
	v_cvt_pk_bf16_f32 v8, v40, v41
	ds_write_b32 v216, v8 offset:5120
	v_cvt_pk_bf16_f32 v8, v42, v43
	ds_write_b32 v216, v8 offset:5376
	v_cvt_pk_bf16_f32 v8, v44, v45
	ds_write_b32 v216, v8 offset:5632
	v_cvt_pk_bf16_f32 v8, v46, v47
	ds_write_b32 v216, v8 offset:5888
	v_cvt_pk_bf16_f32 v8, v16, v17
	ds_write_b32 v216, v8 offset:6144
	v_cvt_pk_bf16_f32 v8, v18, v19
	ds_write_b32 v216, v8 offset:6400
	v_cvt_pk_bf16_f32 v8, v20, v21
	v_mul_f32_e32 v23, v23, v70
	ds_write_b32 v216, v8 offset:6656
	v_cvt_pk_bf16_f32 v8, v22, v23
	ds_write_b32 v216, v8 offset:6912
	v_cvt_pk_bf16_f32 v0, v0, v1
	ds_write_b32 v216, v0 offset:7168
	v_cvt_pk_bf16_f32 v0, v2, v3
	ds_write_b32 v216, v0 offset:7424
	v_cvt_pk_bf16_f32 v0, v4, v5
	ds_write_b32 v216, v0 offset:7680
	v_cvt_pk_bf16_f32 v0, v6, v7
	s_mov_b32 s0, -1
	ds_write_b32 v216, v0 offset:7936
	v_mov_b32_e32 v5, v161
	v_mbcnt_lo_u32_b32 v0, s0, 0
	v_mbcnt_hi_u32_b32 v0, s0, v0
	v_or_b32_e32 v68, s55, v0
	s_movk_i32 s0, 0xffe0
	v_ashrrev_i32_e32 v0, 1, v68
	v_bfi_b32 v0, s0, v0, v68
	v_ashrrev_i32_e32 v1, 31, v0
	v_lshlrev_b64 v[0:1], 11, v[0:1]
	v_lshrrev_b32_e32 v2, 1, v68
	v_ashrrev_i32_e32 v12, 4, v68
	v_lshl_add_u64 v[0:1], s[34:35], 0, v[0:1]
	v_and_b32_e32 v160, 16, v2
	v_lshlrev_b32_e32 v24, 3, v68
	v_ashrrev_i32_e32 v13, 31, v12
	v_lshl_add_u64 v[0:1], v[0:1], 0, v[160:161]
	v_and_b32_e32 v2, 0x78, v24
	v_lshlrev_b64 v[48:49], 11, v[12:13]
	v_lshl_add_u64 v[0:1], s[30:31], 0, v[48:49]
	v_lshlrev_b32_e32 v4, 1, v2
	v_add_u32_e32 v14, 32, v12
	v_ashrrev_i32_e32 v16, 3, v68
	v_lshl_add_u64 v[18:19], v[0:1], 0, v[4:5]
	s_waitcnt lgkmcnt(0)
	s_barrier
; __device__ __forceinline__ int v_st(int k, int c) { const int kk = (k & ~0xC) | ((k & 4) << 1) | ((k & 8) >> 1); return ((kk >> 3) * 4 + (c >> 5)) * 512 + ((kk & 7) * 32 + (c & 31)) * 2; }
; __device__ __forceinline__ int v_rd_base(int lane) { return ((lane & 3) << 3) | (((lane >> 2) & 3) << 6) | (((lane >> 4) & 1) << 5) | (((lane >> 5) & 1) << 8); }
; #define SLOAD(k0) do { vs0 = *reinterpret_cast<const bf16x8*>(&Vh[(size_t)((k0) + sr) * DM + sc]); vs1 = *reinterpret_cast<const bf16x8*>(&Vh[(size_t)((k0) + 32 + sr) * DM + sc]); \
;     ks = *reinterpret_cast<const bf16x8*>(&Kh[(size_t)((k0) + kr) * DM + kc]); } while (0)
; #define SWRITE(s) do { *(bf16x8*)(V_lds + (s) * SHM_V + vst0) = vs0; *(bf16x8*)(V_lds + (s) * SHM_V + vst1) = vs1; *(bf16x8*)(K_lds + (s) * SHM_K64 + kst) = ks; } while (0)
; #define EX2(x) x = __builtin_amdgcn_exp2f(x)
; __device__ __forceinline__ void diff_pass(const bf16_t* __restrict__ Qb, const bf16_t* __restrict__ Kh, const bf16_t* __restrict__ Vh, int seq, char* lds, f32x16 (&o)[4], const int wave_) {
;     ...
;     const bf16_t* Qw = Qb + (size_t)(wid * 32 + r32) * DM + hi * 8;
; #pragma unroll
;     for (int d0 = 0; d0 < 4; ++d0) qr[d0] = *reinterpret_cast<const bf16x8*>(Qw + d0 * 16);
;     const int sr = tid >> 4, sc = (tid & 15) * 8, vst0 = v_st(sr, sc), vst1 = v_st(32 + sr, sc);
;     const int kr = tid >> 3, kc = (tid & 7) * 8, kst = kswz<64>(kr, kc * 2);
;     const int vb0 = (int)(uintptr_t)V_lds + v_rd_base(lane);
;     bf16x8 vs0, vs1, ks;
;     ...
;     f32x16 pA0, pA1, pB0, pB1, negm; float alA, alB; bf16x8 pa0, pa1, pa2, pa3; const int NT = seq / 64;
;     int s_prev = 0, s_cur = 0, s_next = 1;
;     __syncthreads();
;     SLOAD(0); SWRITE(0); SLOAD(64); __syncthreads();
;     negm = f32x16{};
;     qkt64c(pA0, pA1, K_lds, qr, negm, r32, hi);
;     { const float pm = rowmax32(pA0, pA1); m_reg = pm; alA = 1.f;
; #pragma unroll
;       for (int r = 0; r < 16; ++r) { pA0[r] -= pm; pA1[r] -= pm; negm[r] = -pm; }
; #pragma unroll
;       for (int r = 0; r < 16; ++r) EX2(pA0[r]);
; #pragma unroll
;       for (int r = 0; r < 8; ++r) EX2(pA1[r]); }
;     SWRITE(1); __syncthreads();
	v_ashrrev_i32_e32 v15, 31, v14
	v_ashrrev_i32_e32 v17, 31, v16
	v_lshlrev_b32_e32 v64, 4, v68
	v_lshlrev_b64 v[6:7], 11, v[14:15]
	v_lshlrev_b64 v[50:51], 11, v[16:17]
	v_lshl_add_u64 v[6:7], s[30:31], 0, v[6:7]
	v_and_b32_e32 v20, 0x70, v64
	v_lshl_add_u64 v[8:9], s[28:29], 0, v[50:51]
	v_mov_b32_e32 v21, v161
	v_lshl_add_u64 v[4:5], v[6:7], 0, v[4:5]
	v_lshl_add_u64 v[22:23], v[8:9], 0, v[20:21]
	v_and_b32_e32 v13, 0xfffff0, v12
	v_lshlrev_b32_e32 v15, 1, v12
	v_and_or_b32 v13, v15, 8, v13
	v_lshrrev_b32_e32 v15, 1, v12
	v_lshrrev_b32_e32 v13, 1, v13
	v_bfe_u32 v17, v24, 5, 2
	v_and_b32_e32 v12, 3, v12
	v_or_b32_e32 v13, v13, v17
	v_and_or_b32 v12, v15, 4, v12
	v_lshlrev_b32_e32 v13, 9, v13
	v_lshlrev_b32_e32 v12, 6, v12
	v_and_b32_e32 v15, 48, v64
	v_or3_b32 v222, v13, v12, v15
	v_and_b32_e32 v13, 0xfffff0, v14
	v_lshlrev_b32_e32 v14, 1, v14
	v_and_or_b32 v13, v14, 8, v13
	v_lshrrev_b32_e32 v13, 1, v13
	v_or_b32_e32 v13, v13, v17
	v_add_u32_e32 v70, 0, v222
	s_mov_b32 s0, 0x20000
	v_lshlrev_b32_e32 v13, 9, v13
	v_or3_b32 v223, v13, v12, v15
	v_lshlrev_b32_e32 v12, 7, v16
	v_and_b32_e32 v13, 0x70, v68
	s_mov_b32 s1, 0x30000
	v_bitop3_b32 v224, v20, v12, v13 bitop3:0xde
	v_add_u32_e32 v71, 0, v223
	v_add_u32_e32 v225, 0, v224
	v_and_b32_e32 v69, 31, v68
	v_lshlrev_b32_e32 v12, 7, v69
	v_and_b32_e32 v13, 0x70, v24
	v_bitop3_b32 v227, v160, v12, v13 bitop3:0xde
	v_add_u32_e32 v226, 0, v227
	v_and_b32_e32 v72, 63, v68
	s_mov_b32 s12, 0
	s_mov_b32 s13, s12
	s_mov_b32 s14, s12
	s_mov_b32 s15, s12
	s_mov_b32 s16, s12
	s_mov_b32 s17, s12
	s_mov_b32 s18, s12
	s_mov_b32 s19, s12
	s_mov_b32 s20, s12
	s_mov_b32 s21, s12
	s_mov_b32 s22, s12
	s_mov_b32 s23, s12
	s_mov_b32 s24, s12
	s_mov_b32 s25, s12
	s_mov_b32 s26, s12
	s_mov_b32 s27, s12
	s_cmp_lg_u32 0, -1
	s_mov_b32 s29, 2
	s_mov_b32 s28, -1
	s_mov_b32 s30, 1
	v_mov_b32_e32 v234, 1.0
	v_mov_b32_e32 v219, 0
	s_waitcnt vmcnt(0)
	ds_write_b128 v70, v[178:181]
	v_add_co_u32_e32 v0, vcc, s0, v18
	s_nop 1
	v_addc_co_u32_e32 v1, vcc, 0, v19, vcc
	global_load_dwordx4 v[52:55], v[0:1], off
	v_add_co_u32_e32 v0, vcc, s1, v18
	s_waitcnt vmcnt(2)
	ds_write_b128 v71, v[182:185]
	v_addc_co_u32_e32 v1, vcc, 0, v19, vcc
	s_waitcnt vmcnt(1)
	ds_write_b128 v225, v[186:189] offset:49152
	v_add_co_u32_e32 v2, vcc, s0, v22
	v_and_b32_e32 v8, 0x3fffffc0, v68
	s_nop 0
	v_addc_co_u32_e32 v3, vcc, 0, v23, vcc
	global_load_dwordx4 v[56:59], v[0:1], off
	global_load_dwordx4 v[60:63], v[2:3], off offset:128
	s_waitcnt lgkmcnt(0)
	s_barrier
	ds_read_b128 v[0:3], v226 offset:49152
	ds_read_b128 v[4:7], v226 offset:53248
	s_waitcnt lgkmcnt(1)
	v_mfma_f32_32x32x16_bf16 v[32:47], v[0:3], v[162:165], 0
	v_or_b32_e32 v0, 32, v160
	v_bitop3_b32 v231, v0, v12, v13 bitop3:0xde
	v_add_u32_e32 v228, 0, v231
	v_lshl_add_u32 v217, v8, 2, s39
	s_cselect_b32 s0, 0, 0
	v_lshl_add_u32 v218, v69, 2, v217
	s_waitcnt lgkmcnt(0)
	v_mfma_f32_32x32x16_bf16 v[16:31], v[4:7], v[162:165], 0
	ds_read_b128 v[0:3], v228 offset:49152
	ds_read_b128 v[4:7], v228 offset:53248
	s_waitcnt lgkmcnt(1)
	v_mfma_f32_32x32x16_bf16 v[32:47], v[0:3], v[166:169], v[32:47]
	v_or_b32_e32 v0, 64, v160
	v_bitop3_b32 v232, v0, v12, v13 bitop3:0xde
	v_add_u32_e32 v229, 0, v232
	ds_read_b128 v[0:3], v229 offset:53248
	ds_read_b128 v[8:11], v229 offset:49152
	s_waitcnt lgkmcnt(2)
	v_mfma_f32_32x32x16_bf16 v[16:31], v[4:7], v[166:169], v[16:31]
	v_lshlrev_b32_e32 v4, 3, v72
	v_and_b32_e32 v5, 0xc0, v64
	v_lshlrev_b32_e32 v6, 1, v68
	v_and_or_b32 v5, v4, 24, v5
	v_and_b32_e32 v6, 32, v6
	v_and_b32_e32 v4, 0x100, v4
	v_or3_b32 v220, v5, v6, v4
	s_waitcnt lgkmcnt(0)
	v_mfma_f32_32x32x16_bf16 v[32:47], v[8:11], v[170:173], v[32:47]
	v_or_b32_e32 v4, 0x60, v160
	v_bitop3_b32 v233, v4, v12, v13 bitop3:0xde
	v_add_u32_e32 v230, 0, v233
	ds_read_b128 v[64:67], v230 offset:53248
	ds_read_b128 v[4:7], v230 offset:49152
	s_waitcnt vmcnt(2)
	ds_write_b128 v70, v[52:55] offset:16384
	s_waitcnt vmcnt(1)
	ds_write_b128 v71, v[56:59] offset:16384
	s_waitcnt vmcnt(0)
	ds_write_b128 v225, v[60:63] offset:57344
	v_mfma_f32_32x32x16_bf16 v[16:31], v[0:3], v[170:173], v[16:31]
	v_add_u32_e32 v221, s0, v220
	v_cmp_gt_u32_e64 s[0:1], 32, v72
	s_waitcnt lgkmcnt(0)
	s_barrier
; #define EX2(x) x = __builtin_amdgcn_exp2f(x)
; __device__ __forceinline__ void diff_pass(const bf16_t* __restrict__ Qb, const bf16_t* __restrict__ Kh, const bf16_t* __restrict__ Vh, int seq, char* lds, f32x16 (&o)[4], const int wave_) {
;     ...
;     negm = f32x16{};
;     qkt64c(pA0, pA1, K_lds, qr, negm, r32, hi);
;     { const float pm = rowmax32(pA0, pA1); m_reg = pm; alA = 1.f;
; #pragma unroll
;       for (int r = 0; r < 16; ++r) { pA0[r] -= pm; pA1[r] -= pm; negm[r] = -pm; }
; #pragma unroll
;       for (int r = 0; r < 16; ++r) EX2(pA0[r]);
; #pragma unroll
;       for (int r = 0; r < 8; ++r) EX2(pA1[r]); }
	v_mfma_f32_32x32x16_bf16 v[32:47], v[4:7], v[174:177], v[32:47]
	v_mov_b64_e32 v[0:1], s[12:13]
	v_mov_b64_e32 v[14:15], s[26:27]
	v_mov_b64_e32 v[2:3], s[14:15]
	v_mov_b64_e32 v[4:5], s[16:17]
	v_mov_b64_e32 v[6:7], s[18:19]
	v_mov_b64_e32 v[8:9], s[20:21]
	v_mov_b64_e32 v[10:11], s[22:23]
	v_mfma_f32_32x32x16_bf16 v[16:31], v[64:67], v[174:177], v[16:31]
	s_nop 3
	v_max_f32_e32 v64, v33, v33
	v_max_f32_e32 v65, v32, v32
	v_max_f32_e32 v64, v65, v64
	v_mov_b64_e32 v[12:13], s[24:25]
	s_nop 3
	v_max3_f32 v65, v34, v35, v17
	v_max3_f32 v64, v64, v16, v18
	v_max3_f32 v64, v64, v19, v36
	v_max3_f32 v65, v65, v38, v39
	v_max3_f32 v64, v64, v37, v20
	v_max3_f32 v65, v65, v22, v23
	v_max3_f32 v64, v64, v21, v40
	v_max3_f32 v65, v65, v42, v43
	v_max3_f32 v64, v64, v41, v24
	v_max3_f32 v65, v65, v26, v27
	v_max3_f32 v64, v64, v25, v44
	v_max3_f32 v65, v65, v46, v47
	v_max3_f32 v64, v64, v45, v28
	v_max3_f32 v65, v65, v30, v31
	v_max3_f32 v64, v64, v29, v65
	v_mov_b32_e32 v65, v64
	s_nop 1
	v_permlane32_swap_b32_e32 v64, v65
	v_max_f32_e32 v65, v65, v65
	v_max_f32_e32 v64, v64, v64
	v_max_f32_e32 v196, v64, v65
	v_sub_f32_e32 v18, v18, v196
	v_sub_f32_e32 v16, v16, v196
	v_sub_f32_e32 v17, v17, v196
	v_sub_f32_e32 v19, v19, v196
	v_exp_f32_e32 v114, v18
	v_and_b32_e32 v18, 7, v68
	v_exp_f32_e32 v112, v16
	v_exp_f32_e32 v113, v17
	v_exp_f32_e32 v115, v19
	v_lshl_add_u64 v[16:17], s[10:11], 0, v[50:51]
	v_lshlrev_b32_e32 v18, 4, v18
	v_mov_b32_e32 v19, v161
	v_sub_f32_e32 v32, v32, v196
	v_sub_f32_e32 v33, v33, v196
	v_sub_f32_e32 v34, v34, v196
	v_sub_f32_e32 v35, v35, v196
	v_sub_f32_e32 v36, v36, v196
	v_sub_f32_e32 v20, v20, v196
	v_sub_f32_e32 v37, v37, v196
	v_sub_f32_e32 v21, v21, v196
	v_sub_f32_e32 v38, v38, v196
	v_sub_f32_e32 v22, v22, v196
	v_sub_f32_e32 v39, v39, v196
	v_sub_f32_e32 v23, v23, v196
	v_sub_f32_e32 v40, v40, v196
	v_sub_f32_e32 v41, v41, v196
	v_pk_add_f32 v[120:121], v[24:25], v[196:197] op_sel_hi:[1,0] neg_lo:[0,1] neg_hi:[0,1]
	v_sub_f32_e32 v24, v42, v196
	v_sub_f32_e32 v25, v43, v196
	v_pk_add_f32 v[122:123], v[26:27], v[196:197] op_sel_hi:[1,0] neg_lo:[0,1] neg_hi:[0,1]
	v_sub_f32_e32 v26, v44, v196
	v_sub_f32_e32 v27, v45, v196
	v_pk_add_f32 v[124:125], v[28:29], v[196:197] op_sel_hi:[1,0] neg_lo:[0,1] neg_hi:[0,1]
	v_sub_f32_e32 v28, v46, v196
	v_sub_f32_e32 v29, v47, v196
	v_lshl_add_u64 v[16:17], v[16:17], 0, v[18:19]
	v_and_b32_e32 v18, 15, v68
	v_exp_f32_e32 v96, v32
	v_exp_f32_e32 v97, v33
	v_exp_f32_e32 v98, v34
	v_exp_f32_e32 v99, v35
	v_exp_f32_e32 v100, v36
	v_exp_f32_e32 v101, v37
	v_exp_f32_e32 v102, v38
	v_exp_f32_e32 v103, v39
	v_exp_f32_e32 v104, v40
	v_exp_f32_e32 v105, v41
	v_exp_f32_e32 v106, v24
	v_exp_f32_e32 v107, v25
	v_exp_f32_e32 v108, v26
	v_exp_f32_e32 v109, v27
	v_exp_f32_e32 v110, v28
	v_exp_f32_e32 v111, v29
	v_exp_f32_e32 v116, v20
	v_exp_f32_e32 v117, v21
	v_exp_f32_e32 v118, v22
	v_exp_f32_e32 v119, v23
	v_lshl_add_u64 v[198:199], s[52:53], 0, v[16:17]
	v_lshl_add_u64 v[16:17], s[10:11], 0, v[48:49]
	v_lshlrev_b32_e32 v18, 4, v18
	v_lshl_add_u64 v[16:17], v[16:17], 0, v[18:19]
	v_xor_b32_e32 v80, 0x80000000, v196
	v_pk_add_f32 v[126:127], v[30:31], v[196:197] op_sel_hi:[1,0] neg_lo:[0,1] neg_hi:[0,1]
	v_lshl_add_u64 v[200:201], s[52:53], 0, v[16:17]
	s_add_u32 s14, s52, s10
	s_addc_u32 s15, s53, s11
	s_add_u32 s14, s14, s64
	s_addc_u32 s15, s15, s65
	s_add_u32 s16, s14, 0x8a40000
	s_addc_u32 s17, s15, 0
	s_add_u32 s14, s14, 0x6a40080
	s_addc_u32 s15, s15, 0
	s_lshl_b32 s18, s55, 4
	s_cmp_lt_u32 s18, 0x1000
	s_cbranch_scc0 .Lprio_p2_skip
	s_setprio 2

; __device__ __forceinline__ int fresh_lane() { unsigned m = ~0u; asm volatile("" : "+s"(m)); return (int)__builtin_amdgcn_mbcnt_hi(m, __builtin_amdgcn_mbcnt_lo(m, 0u)); }
; #define GRID_BAR() do { } while (0)
; #define GRID_BAR() do { xcd_barrier(bar); if ((PROBE_MASK >> 12) & 1) xcd_barrier(bar); } while (0)
; #define SEAM(k) do { if (IN(k) && IN((k) + 1)) GRID_BAR(); } while (0)
; __device__ __forceinline__ void xcd_barrier(const XcdBarrier& b) {
;     asm volatile("s_waitcnt vmcnt(0)" ::: "memory");
;     __syncthreads();
;     if (b.wave == 0 && fresh_lane() == 0) {
;         unsigned* bar = b.bar; unsigned bx_ = b.x;
;         asm volatile("" : "+s"(bar), "+s"(bx_));
;         __builtin_amdgcn_s_waitcnt(0);
;         unsigned nloc = b.st[0], nx = b.st[1];
;         if (nloc == 0u) { xcd_barrier_complete(bar, bx_, nloc, nx); b.st[0] = nloc; b.st[1] = nx; }
; __global__ void __launch_bounds__(512, 2) fwd(Args args) {
;     ...
;             __syncthreads();
;         } if (rep_ + 1 < NREP(1)) GRID_BAR(); }
;         SEAM(pb + 1);
.LBB0_870:
	s_setprio 0
	s_barrier
	s_waitcnt vmcnt(0)
	v_readlane_b32 s0, v251, 8
	v_readlane_b32 s1, v251, 9
	s_and_b64 vcc, exec, s[0:1]
	s_barrier
	s_cbranch_vccz .LBB0_916
	s_mov_b32 s0, -1
	s_nop 0
	v_mbcnt_lo_u32_b32 v0, s0, 0
	v_mbcnt_hi_u32_b32 v0, s0, v0
	v_cmp_eq_u32_e32 vcc, 0, v0
	s_and_saveexec_b64 s[36:37], vcc
	s_cbranch_execz .LBB0_915
	v_readlane_b32 s38, v251, 5
	v_readlane_b32 s0, v252, 35
	v_readlane_b32 s39, v251, 6
	v_readlane_b32 s2, v251, 7
	v_mov_b32_e32 v0, s0
	s_waitcnt vmcnt(0) expcnt(0) lgkmcnt(0)
	ds_read_b32 v2, v0
	v_readlane_b32 s0, v252, 36
	s_waitcnt lgkmcnt(0)
	v_cmp_ne_u32_e32 vcc, 0, v2
	v_mov_b32_e32 v0, s0
	ds_read_b32 v0, v0
	s_cbranch_vccnz .LBB0_886
	v_readlane_b32 s0, v251, 0
	v_readlane_b32 s1, v251, 1
	s_load_dwordx2 s[6:7], s[0:1], 0x4
	s_add_u32 s0, s38, 0x1000
	s_addc_u32 s1, s39, 0
	s_add_u32 s4, s38, 0x1100
	s_addc_u32 s5, s39, 0
	v_readlane_b32 s3, v251, 2
	s_waitcnt lgkmcnt(0)
	s_mul_i32 s3, s6, s3
	s_add_u32 s6, s38, 0x1200
	s_mul_i32 s3, s3, s7
	s_addc_u32 s7, s39, 0
	s_add_u32 s10, s38, 0x1300
	s_addc_u32 s11, s39, 0
	s_mov_b32 s8, 1
	s_mov_b64 s[12:13], 0
	s_branch .LBB0_876
